# MoE gate-up unit order variant: each XCD takes 4 row panels x 8 weight tiles per round (was 8 x 4)
# baseline (speedup 1.0000x reference)
; #define LAS __attribute__((address_space(3)))
;     __device__ __forceinline__ void init(const int* moe_base, int N, int G_, int c_) { nP = __builtin_amdgcn_readfirstlane(moe_base[8]) >> 8; nN = N / 256; nU = nP * nN; G = G_; c = c_;
;         b1 = __builtin_amdgcn_readfirstlane(moe_base[1]); b2 = __builtin_amdgcn_readfirstlane(moe_base[2]); b3 = __builtin_amdgcn_readfirstlane(moe_base[3]); b4 = __builtin_amdgcn_readfirstlane(moe_base[4]);
;         b5 = __builtin_amdgcn_readfirstlane(moe_base[5]); b6 = __builtin_amdgcn_readfirstlane(moe_base[6]); b7 = __builtin_amdgcn_readfirstlane(moe_base[7]); }
;     __device__ __forceinline__ bool next(int i, pg8::Unit& u) const {
;         const int L = i * G + c; if (L >= nU) return false;
;         const int nig = 8 * nN, gid = L / nig, fm = gid * 8, gsz = (nP - fm) < 8 ? (nP - fm) : 8, r = L % nig;
;         u.pm = fm + r % gsz; u.pn = r / gsz;
;         const int row0 = u.pm * 256; const int e = (row0 >= b1) + (row0 >= b2) + (row0 >= b3) + (row0 >= b4) + (row0 >= b5) + (row0 >= b6) + (row0 >= b7);
;         u.pb = e * nN + u.pn; return true;
; __global__ void __launch_bounds__(512, 2) mk_fwd(Args a) {
;     extern __shared__ __attribute__((aligned(16))) unsigned char lds_raw[];
;     LAS unsigned char* lds = (LAS unsigned char*)lds_raw;
;     volatile LAS unsigned* MISC = (volatile LAS unsigned*)(lds + MISC_OFF);
;     if (threadIdx.x < 64) MISC[threadIdx.x] = 0u;
;     __syncthreads();
;     const int lo = a.ph_lo, hi = a.ph_hi;
;     ...
;     XcdBarrier bar = xcd_barrier_post((unsigned*)(a.ws + WS_CTL) + CW_BAR, MISC + 8);
_Z6mk_fwd4Args:
	s_load_dwordx8 s[60:67], s[0:1], 0xc0
	v_writelane_b32 v255, s2, 0
	s_and_b32 s99, s2, 7
	s_lshr_b32 s100, s2, 3
	s_lshr_b32 s98, s99, 1
	s_lshl_b32 s98, s98, 6
	s_and_b32 s99, s99, 1
	s_lshl_b32 s99, s99, 2
	s_or_b32 s98, s98, s99
	s_lshr_b32 s99, s100, 2
	s_lshl_b32 s99, s99, 3
	s_or_b32 s98, s98, s99
	s_and_b32 s99, s100, 3
	s_or_b32 s99, s98, s99
	s_load_dword s98, s[0:1], 0xf0
	s_waitcnt lgkmcnt(0)
	s_cmp_eq_u32 s98, 0x100
	s_cselect_b32 s99, s99, s2
	v_writelane_b32 v255, s99, 62
	v_writelane_b32 v255, s0, 1
	s_load_dwordx2 s[4:5], s[0:1], 0xe0
	v_cmp_gt_u32_e32 vcc, 64, v0
	v_writelane_b32 v255, s1, 2
	s_and_saveexec_b64 s[0:1], vcc
	v_lshl_add_u32 v1, v0, 2, 0
	v_add_u32_e32 v1, 0x24400, v1
	v_mov_b32_e32 v2, 0
	ds_write_b32 v1, v2
	s_waitcnt lgkmcnt(0)
	v_writelane_b32 v255, s4, 3
	s_nop 1
	v_writelane_b32 v255, s5, 4
	s_or_b64 exec, exec, s[0:1]
	s_add_u32 s0, s66, 0x4000
	s_addc_u32 s1, s67, 0
	v_writelane_b32 v255, s0, 5
	s_barrier
	s_nop 0
	v_writelane_b32 v255, s1, 6
	s_getreg_b32 s0, hwreg(HW_REG_XCC_ID, 0, 4)
	s_and_b32 s0, s0, 15
	v_writelane_b32 v255, s0, 7
	v_cmp_ne_u32_e64 s[0:1], 0, v0
	v_cmp_eq_u32_e64 s[2:3], 0, v0
	s_nop 0
	v_writelane_b32 v255, s0, 8
	s_nop 1
	v_writelane_b32 v255, s1, 9
	s_mov_b64 s[0:1], exec
	v_writelane_b32 v255, s2, 10
	s_nop 1
	v_writelane_b32 v255, s3, 11
	s_and_b64 s[2:3], s[0:1], s[2:3]
	s_mov_b64 exec, s[2:3]
	s_cbranch_execz .LBB0_5
	s_mov_b64 s[2:3], exec
	v_mbcnt_lo_u32_b32 v1, s2, 0
	v_mbcnt_hi_u32_b32 v1, s3, v1
	v_cmp_eq_u32_e32 vcc, 0, v1
	s_and_b64 s[4:5], exec, vcc
	s_mov_b64 exec, s[4:5]
	s_cbranch_execz .LBB0_5
	v_readlane_b32 s4, v255, 7
	s_bcnt1_i32_b64 s2, s[2:3]
	s_lshl_b32 s4, s4, 8
	v_mov_b32_e32 v2, s2
	v_readlane_b32 s2, v255, 5
	v_mov_b32_e32 v1, s4
	v_readlane_b32 s3, v255, 6
	s_nop 4
	global_atomic_add v1, v2, s[2:3] offset:1024
